# grid barrier: leader waits for its L1 invalidate again (acquire must complete before the workgroup barrier); per-XCD relay and its add stay removed
# baseline (speedup 1.0000x reference)
.LBB0_269:
	s_or_b64 exec, exec, s[6:7]
	s_mov_b64 s[6:7], exec
	v_mbcnt_lo_u32_b32 v1, s6, 0
	v_mbcnt_hi_u32_b32 v1, s7, v1
	v_cmp_eq_u32_e32 vcc, 0, v1
	buffer_inv sc1
	s_waitcnt vmcnt(0)
	s_and_saveexec_b64 s[8:9], vcc
	s_cbranch_execz .LBB0_271
	s_bcnt1_i32_b64 s2, s[6:7]
	v_mov_b32_e32 v1, 0x2000
	v_mov_b32_e32 v2, s2

.LBB0_815:
	s_or_b64 exec, exec, s[8:9]
	s_mov_b64 s[8:9], exec
	v_mbcnt_lo_u32_b32 v1, s8, 0
	v_mbcnt_hi_u32_b32 v1, s9, v1
	v_cmp_eq_u32_e32 vcc, 0, v1
	buffer_inv sc1
	s_waitcnt vmcnt(0)
	s_and_saveexec_b64 s[10:11], vcc
	s_cbranch_execz .LBB0_817
	s_bcnt1_i32_b64 s8, s[8:9]
	v_mov_b32_e32 v1, 0x2000
	v_mov_b32_e32 v2, s8

.LBB0_983:
	s_or_b64 exec, exec, s[6:7]
	s_mov_b64 s[6:7], exec
	v_mbcnt_lo_u32_b32 v1, s6, 0
	v_mbcnt_hi_u32_b32 v1, s7, v1
	v_cmp_eq_u32_e32 vcc, 0, v1
	buffer_inv sc1
	s_waitcnt vmcnt(0)
	s_and_saveexec_b64 s[8:9], vcc
	s_cbranch_execz .LBB0_985
	s_bcnt1_i32_b64 s6, s[6:7]
	v_mov_b32_e32 v1, 0x2000
	v_mov_b32_e32 v2, s6

.LBB0_1161:
	s_or_b64 exec, exec, s[10:11]
	s_mov_b64 s[10:11], exec
	v_mbcnt_lo_u32_b32 v1, s10, 0
	v_mbcnt_hi_u32_b32 v1, s11, v1
	v_cmp_eq_u32_e32 vcc, 0, v1
	buffer_inv sc1
	s_waitcnt vmcnt(0)
	s_and_saveexec_b64 s[12:13], vcc
	s_cbranch_execz .LBB0_1163
	s_bcnt1_i32_b64 s10, s[10:11]
	v_mov_b32_e32 v1, 0x2000
	v_mov_b32_e32 v2, s10
